# baseline (speedup 1.0000x reference)
_Z11gemm_8phaseILi0ELi16ELi16ELi1024ELi1024ELi4096ELi1EEvPKDF16_S1_PvS2_fPj:
	s_load_dwordx4 s[4:7], s[0:1], 0x0
	s_and_b32 s3, s2, 7
	s_lshl_b32 s3, s3, 5
	s_lshr_b32 s8, s2, 3
	s_add_i32 s2, s3, s8
	s_and_b32 s3, s2, 127
	s_lshr_b32 s8, s2, 7
	s_lshl_b32 s8, s8, 3
	s_and_b32 s9, s3, 7
	s_add_i32 s10, s8, s9
	s_lshr_b32 s3, s3, 3
	s_mov_b32 s9, s3
	s_mov_b32 s8, 0
	v_lshrrev_b32_e32 v2, 3, v0
	v_and_b32_e32 v4, 48, v2
	v_bfe_u32 v5, v0, 2, 4
	s_lshl_b32 s28, s10, 8
	v_or_b32_e32 v9, v4, v5
	v_or_b32_e32 v2, s28, v9
	s_lshl_b32 s29, s3, 7
	v_ashrrev_i32_e32 v3, 31, v2
	v_lshlrev_b64 v[10:11], 11, v[2:3]
	v_or_b32_e32 v2, s29, v9
	v_lshlrev_b32_e32 v6, 4, v0
	v_and_b32_e32 v1, 32, v0
	v_ashrrev_i32_e32 v3, 31, v2
	s_add_i32 s10, 0, 0x10000
	v_bitop3_b32 v7, v6, v1, 48 bitop3:0x6c
	v_and_b32_e32 v8, 64, v0
	v_lshlrev_b64 v[2:3], 11, v[2:3]
	v_add_u32_e32 v145, s10, v6
	v_or_b32_e32 v130, v7, v8
	v_mov_b32_e32 v131, 0
	s_waitcnt lgkmcnt(0)
	v_lshl_add_u64 v[2:3], s[6:7], 0, v[2:3]
	v_readfirstlane_b32 s2, v145
	v_add_u32_e32 v146, 0x2000, v145
	v_lshl_add_u64 v[2:3], v[2:3], 0, v[130:131]
	s_mov_b32 m0, s2
	s_mov_b64 s[2:3], 0x20000
	v_readfirstlane_b32 s11, v146
	v_lshl_add_u64 v[10:11], s[4:5], 0, v[10:11]
	v_add_u32_e32 v144, 0, v6
	global_load_lds_dwordx4 v[2:3], off
	v_lshl_add_u64 v[12:13], v[2:3], 0, s[2:3]
	s_mov_b32 m0, s11
	v_lshl_add_u64 v[132:133], v[10:11], 0, v[130:131]
	v_readfirstlane_b32 s11, v144
	v_add_u32_e32 v147, 0x2000, v144
	global_load_lds_dwordx4 v[12:13], off
	s_mov_b32 m0, s11
	v_lshl_add_u64 v[10:11], v[132:133], 0, s[2:3]
	v_readfirstlane_b32 s2, v147
	s_add_i32 s11, 0, 0x14000
	global_load_lds_dwordx4 v[132:133], off
	s_mov_b32 m0, s2
	v_add_u32_e32 v149, s11, v6
	s_mov_b64 s[2:3], 0x400000
	global_load_lds_dwordx4 v[10:11], off
	v_lshl_add_u64 v[10:11], v[2:3], 0, s[2:3]
	v_readfirstlane_b32 s2, v149
	s_mov_b32 m0, s2
	s_mov_b64 s[2:3], 0x420000
	v_add_u32_e32 v150, 0x2000, v149
	global_load_lds_dwordx4 v[10:11], off
	v_lshl_add_u64 v[10:11], v[2:3], 0, s[2:3]
	v_readfirstlane_b32 s2, v150
	s_mov_b32 m0, s2
	v_add_u32_e32 v151, 0x4000, v144
	s_mov_b64 s[2:3], 0x40000
	global_load_lds_dwordx4 v[10:11], off
	v_lshl_add_u64 v[10:11], v[132:133], 0, s[2:3]
	v_readfirstlane_b32 s2, v151
	s_mov_b32 m0, s2
	s_mov_b64 s[2:3], 0x60000
	v_add_u32_e32 v153, 0x6000, v144
	global_load_lds_dwordx4 v[10:11], off
	v_lshl_add_u64 v[10:11], v[132:133], 0, s[2:3]
	v_readfirstlane_b32 s2, v153
	s_mov_b32 m0, s2
	v_lshrrev_b32_e32 v9, 8, v0
	global_load_lds_dwordx4 v[10:11], off
	v_cmp_eq_u32_e32 vcc, 1, v9
	s_and_saveexec_b64 s[2:3], vcc
	s_cbranch_execz .LBB5_6
	s_barrier
